# NA per-wave dead-tile skip + KV-split rebalanced to KS0=236/KS1=212 (upper WGs have less NA work)
# baseline (speedup 1.0000x reference)
.Lkv_latch:
	s_cmp_eq_u32 s31, 2
	s_cbranch_scc1 .LBB0_597
	s_mov_b32 s31, 2
	v_readlane_b32 s19, v254, 0
	s_nop 3
	s_cmpk_lt_u32 s19, 0x80
	s_cbranch_scc1 .Lkv_lower2
	s_add_i32 s19, s19, 0x80
	s_mov_b32 s30, 1
	s_cmp_eq_u32 s32, 1
	s_cbranch_scc1 .Lkv_upL0
	s_mov_b32 s28, 0x7740000
	s_movk_i32 s29, 44
	s_branch .LBB0_584
.Lkv_upL0:
	s_mov_b32 s28, 0x84c0000
	s_movk_i32 s29, 20
	s_cmpk_gt_u32 s19, 0x10f
	s_cbranch_scc1 .LBB0_584
	s_mov_b32 s28, 0x8700000
	s_movk_i32 s29, 16
	s_branch .LBB0_584
.Lkv_lower2:
	s_add_i32 s19, s19, 0x100
	s_mov_b32 s28, 0
	s_mov_b32 s30, 2
	s_cmp_eq_u32 s32, 1
	s_cbranch_scc1 .Lkv_loL0
	s_movk_i32 s29, 208
	s_branch .LBB0_584
.Lkv_loL0:
	s_movk_i32 s29, 232
	s_cmpk_gt_u32 s19, 0x10f
	s_cbranch_scc1 .LBB0_584
	s_movk_i32 s29, 236
	s_branch .LBB0_584
